# speedup vs baseline: 1.0097x; 1.0097x over previous
.LBB1_2:
	s_cmp_gt_i32 s38, 29
	s_cbranch_scc1 .LBB1_31
	s_add_i32 s18, s38, 4
	s_add_i32 s4, s33, s18
	s_cmp_eq_u32 s4, 4
	s_mov_b64 s[8:9], -1
	s_cbranch_scc0 .LBB1_5

.LBB1_23:
	s_add_i32 s38, s38, 2
	s_add_i32 s18, s18, 2
	s_mov_b64 s[8:9], 0
	s_cmp_gt_i32 s38, 29
	s_cbranch_scc1 .LBB1_32
